# baseline (speedup 1.0000x reference)
.Lmy_wg_skip:
	s_or_b64 exec, exec, s[16:17]
	global_load_dwordx4 v[44:47], v[20:21], off offset:144
	global_load_dwordx4 v[56:59], v[20:21], off offset:128
	global_load_dwordx4 v[0:3], v[20:21], off offset:208
	global_load_dwordx4 v[8:11], v[20:21], off offset:192
	global_load_dwordx4 v[4:7], v[20:21], off offset:272
	global_load_dwordx4 v[12:15], v[20:21], off offset:256
	v_lshl_add_u64 v[16:17], s[8:9], 0, v[72:73]
	v_lshlrev_b32_e32 v72, 4, v141
	v_lshl_add_u64 v[16:17], v[16:17], 0, v[72:73]
	v_mad_u32_u24 v74, v76, s4, v72
	global_load_dwordx4 v[156:159], v[16:17], off
	global_load_dwordx4 v[152:155], v[16:17], off offset:32
	global_load_dwordx4 v[148:151], v[16:17], off offset:64
	global_load_dwordx4 v[144:147], v[16:17], off offset:96
	global_load_dwordx4 v[32:35], v[20:21], off offset:336
	global_load_dwordx4 v[36:39], v[20:21], off offset:320
	global_load_dwordx4 v[24:27], v[20:21], off offset:400
	global_load_dwordx4 v[28:31], v[20:21], off offset:384
	s_nop 0
	global_load_dwordx4 v[16:19], v[20:21], off offset:464
	s_nop 0
	global_load_dwordx4 v[20:23], v[20:21], off offset:448
	s_waitcnt lgkmcnt(0)
	s_barrier
	ds_read_b128 v[68:71], v74
	s_mov_b32 s3, 0x43800000
	v_fma_mix_f32 v143, v64, s3, -v60 op_sel_hi:[0,0,1]
	v_fma_mix_f32 v160, v65, s3, -v60 op_sel:[0,0,1] op_sel_hi:[0,0,1]
	v_fma_mix_f32 v161, v66, s3, -v61 op_sel_hi:[0,0,1]
	v_fma_mix_f32 v162, v67, s3, -v61 op_sel:[0,0,1] op_sel_hi:[0,0,1]
	ds_read_b128 v[64:67], v74 offset:32
	s_waitcnt lgkmcnt(1)
	v_mfma_f32_32x32x16_f16 a[16:31], v[60:63], v[68:71], 0
	v_fma_mix_f32 v163, v40, s3, -v62 op_sel_hi:[0,0,1]
	v_fma_mix_f32 v43, v43, s3, -v63 op_sel:[0,0,1] op_sel_hi:[0,0,1]
	v_fma_mix_f32 v164, v41, s3, -v62 op_sel:[0,0,1] op_sel_hi:[0,0,1]
	v_fma_mix_f32 v165, v42, s3, -v63 op_sel_hi:[0,0,1]
	v_cvt_pk_f16_f32 v40, v143, v160
	v_cvt_pk_f16_f32 v41, v161, v162
	v_cvt_pk_f16_f32 v42, v163, v164
	v_cvt_pk_f16_f32 v43, v165, v43
	s_nop 0
	v_mfma_f32_32x32x16_f16 a[16:31], v[40:43], v[68:71], a[16:31]
	ds_read_b128 v[68:71], v74 offset:8704
	ds_read_b128 v[160:163], v74 offset:8736
	s_waitcnt lgkmcnt(1)
	v_mfma_f32_32x32x16_f16 a[0:15], v[60:63], v[68:71], 0
	v_mfma_f32_32x32x16_f16 a[0:15], v[40:43], v[68:71], a[0:15]
	v_mov_b32_e32 v40, 0x4400
	v_mad_u32_u24 v41, v76, s4, v40
	v_add_u32_e32 v40, v41, v72
	ds_read_b128 v[68:71], v40
	ds_read_b128 v[164:167], v40 offset:32
	s_waitcnt vmcnt(18)
	v_mul_f32_e32 v42, 0x43800000, v52
	v_mul_f32_e32 v43, 0x43800000, v53
	s_waitcnt lgkmcnt(1)
	v_mfma_f32_32x32x16_f16 a[16:31], v[60:63], v[68:71], a[16:31]
	ds_read_b128 v[68:71], v40 offset:8704
	ds_read_b128 v[168:171], v40 offset:8736
	s_waitcnt lgkmcnt(1)
	v_mfma_f32_32x32x16_f16 a[0:15], v[60:63], v[68:71], a[0:15]
	v_mul_f32_e32 v61, 0x43800000, v54
	v_mul_f32_e32 v62, 0x43800000, v55
	v_cvt_pk_f16_f32 v60, v42, v43
	v_cvt_pk_f16_f32 v61, v61, v62
	s_nop 0
	v_fma_mix_f32 v42, v52, s3, -v60 op_sel_hi:[0,0,1]
	v_fma_mix_f32 v43, v53, s3, -v60 op_sel:[0,0,1] op_sel_hi:[0,0,1]
	v_fma_mix_f32 v52, v54, s3, -v61 op_sel_hi:[0,0,1]
	v_fma_mix_f32 v53, v55, s3, -v61 op_sel:[0,0,1] op_sel_hi:[0,0,1]
	s_waitcnt vmcnt(17)
	v_mul_f32_e32 v54, 0x43800000, v48
	v_mul_f32_e32 v55, 0x43800000, v49
	v_cvt_pk_f16_f32 v62, v54, v55
	v_mul_f32_e32 v54, 0x43800000, v50
	v_mul_f32_e32 v55, 0x43800000, v51
	v_cvt_pk_f16_f32 v63, v54, v55
	v_fma_mix_f32 v54, v48, s3, -v62 op_sel_hi:[0,0,1]
	v_mfma_f32_32x32x16_f16 a[16:31], v[60:63], v[64:67], a[16:31]
	v_fma_mix_f32 v51, v51, s3, -v63 op_sel:[0,0,1] op_sel_hi:[0,0,1]
	v_fma_mix_f32 v55, v49, s3, -v62 op_sel:[0,0,1] op_sel_hi:[0,0,1]
	v_fma_mix_f32 v68, v50, s3, -v63 op_sel_hi:[0,0,1]
	v_cvt_pk_f16_f32 v48, v42, v43
	v_cvt_pk_f16_f32 v49, v52, v53
	v_cvt_pk_f16_f32 v50, v54, v55
	v_cvt_pk_f16_f32 v51, v68, v51
	v_mfma_f32_32x32x16_f16 a[0:15], v[60:63], v[160:163], a[0:15]
	ds_read_b128 v[52:55], v74 offset:64
	s_waitcnt vmcnt(14)
	v_mul_f32_e32 v42, 0x43800000, v56
	v_mul_f32_e32 v43, 0x43800000, v57
	v_mfma_f32_32x32x16_f16 a[16:31], v[48:51], v[64:67], a[16:31]
	v_mfma_f32_32x32x16_f16 a[0:15], v[48:51], v[160:163], a[0:15]
	v_mul_f32_e32 v49, 0x43800000, v58
	v_mul_f32_e32 v50, 0x43800000, v59
	v_cvt_pk_f16_f32 v49, v49, v50
	v_mul_f32_e32 v50, 0x43800000, v44
	v_mul_f32_e32 v51, 0x43800000, v45
	v_cvt_pk_f16_f32 v48, v42, v43
	v_cvt_pk_f16_f32 v50, v50, v51
	v_mfma_f32_32x32x16_f16 a[16:31], v[60:63], v[164:167], a[16:31]
	v_fma_mix_f32 v42, v56, s3, -v48 op_sel_hi:[0,0,1]
	v_mul_f32_e32 v51, 0x43800000, v46
	v_mul_f32_e32 v56, 0x43800000, v47
	v_fma_mix_f32 v43, v57, s3, -v48 op_sel:[0,0,1] op_sel_hi:[0,0,1]
	v_cvt_pk_f16_f32 v51, v51, v56
	v_fma_mix_f32 v44, v44, s3, -v50 op_sel_hi:[0,0,1]
	v_fma_mix_f32 v45, v45, s3, -v50 op_sel:[0,0,1] op_sel_hi:[0,0,1]
	s_waitcnt lgkmcnt(1)
	v_mfma_f32_32x32x16_f16 a[0:15], v[60:63], v[168:171], a[0:15]
	v_fma_mix_f32 v60, v58, s3, -v49 op_sel_hi:[0,0,1]
	v_fma_mix_f32 v61, v59, s3, -v49 op_sel:[0,0,1] op_sel_hi:[0,0,1]
	ds_read_b128 v[56:59], v74 offset:96
	v_fma_mix_f32 v46, v46, s3, -v51 op_sel_hi:[0,0,1]
	v_fma_mix_f32 v47, v47, s3, -v51 op_sel:[0,0,1] op_sel_hi:[0,0,1]
	v_cvt_pk_f16_f32 v42, v42, v43
	v_cvt_pk_f16_f32 v43, v60, v61
	s_waitcnt lgkmcnt(1)
	v_mfma_f32_32x32x16_f16 a[16:31], v[48:51], v[52:55], a[16:31]
	v_cvt_pk_f16_f32 v44, v44, v45
	v_cvt_pk_f16_f32 v45, v46, v47
	s_waitcnt vmcnt(13)
	v_mul_f32_e32 v46, 0x43800000, v3
	v_mfma_f32_32x32x16_f16 a[16:31], v[42:45], v[52:55], a[16:31]
	ds_read_b128 v[52:55], v74 offset:8768
	ds_read_b128 v[60:63], v74 offset:8800
	s_waitcnt lgkmcnt(1)
	v_mfma_f32_32x32x16_f16 a[0:15], v[48:51], v[52:55], a[0:15]
	v_mfma_f32_32x32x16_f16 a[0:15], v[42:45], v[52:55], a[0:15]
	ds_read_b128 v[42:45], v40 offset:64
	ds_read_b128 v[52:55], v40 offset:96
	s_waitcnt lgkmcnt(1)
	v_mfma_f32_32x32x16_f16 a[16:31], v[48:51], v[42:45], a[16:31]
	ds_read_b128 v[42:45], v40 offset:8768
	ds_read_b128 v[64:67], v40 offset:8800
	s_waitcnt lgkmcnt(1)
	v_mfma_f32_32x32x16_f16 a[0:15], v[48:51], v[42:45], a[0:15]
	s_waitcnt vmcnt(12)
	v_mul_f32_e32 v42, 0x43800000, v8
	v_mul_f32_e32 v43, 0x43800000, v9
	v_mul_f32_e32 v44, 0x43800000, v10
	v_mul_f32_e32 v45, 0x43800000, v11
	v_cvt_pk_f16_f32 v42, v42, v43
	v_cvt_pk_f16_f32 v43, v44, v45
	v_mul_f32_e32 v44, 0x43800000, v0
	v_mul_f32_e32 v45, 0x43800000, v1
	v_cvt_pk_f16_f32 v44, v44, v45
	v_mul_f32_e32 v45, 0x43800000, v2
	v_cvt_pk_f16_f32 v45, v45, v46
	v_fma_mix_f32 v8, v8, s3, -v42 op_sel_hi:[0,0,1]
	v_fma_mix_f32 v3, v3, s3, -v45 op_sel:[0,0,1] op_sel_hi:[0,0,1]
	v_mfma_f32_32x32x16_f16 a[16:31], v[42:45], v[56:59], a[16:31]
	v_fma_mix_f32 v9, v9, s3, -v42 op_sel:[0,0,1] op_sel_hi:[0,0,1]
	v_fma_mix_f32 v10, v10, s3, -v43 op_sel_hi:[0,0,1]
	v_fma_mix_f32 v11, v11, s3, -v43 op_sel:[0,0,1] op_sel_hi:[0,0,1]
	v_fma_mix_f32 v46, v0, s3, -v44 op_sel_hi:[0,0,1]
	v_fma_mix_f32 v47, v1, s3, -v44 op_sel:[0,0,1] op_sel_hi:[0,0,1]
	v_fma_mix_f32 v48, v2, s3, -v45 op_sel_hi:[0,0,1]
	v_cvt_pk_f16_f32 v0, v8, v9
	v_cvt_pk_f16_f32 v1, v10, v11
	v_cvt_pk_f16_f32 v2, v46, v47
	v_cvt_pk_f16_f32 v3, v48, v3
	s_waitcnt vmcnt(10)
	v_mul_f32_e32 v8, 0x43800000, v12
	v_mfma_f32_32x32x16_f16 a[16:31], v[0:3], v[56:59], a[16:31]
	v_mul_f32_e32 v9, 0x43800000, v13
	v_mul_f32_e32 v10, 0x43800000, v14
	v_mul_f32_e32 v11, 0x43800000, v15
	v_cvt_pk_f16_f32 v8, v8, v9
	v_cvt_pk_f16_f32 v9, v10, v11
	v_mul_f32_e32 v10, 0x43800000, v4
	v_fma_mix_f32 v50, v12, s3, -v8 op_sel_hi:[0,0,1]
	v_mfma_f32_32x32x16_f16 a[16:31], v[42:45], v[52:55], a[16:31]
	v_fma_mix_f32 v51, v13, s3, -v8 op_sel:[0,0,1] op_sel_hi:[0,0,1]
	v_fma_mix_f32 v52, v14, s3, -v9 op_sel_hi:[0,0,1]
	v_fma_mix_f32 v53, v15, s3, -v9 op_sel:[0,0,1] op_sel_hi:[0,0,1]
	ds_read_b128 v[12:15], v74 offset:128
	v_mul_f32_e32 v11, 0x43800000, v5
	v_cvt_pk_f16_f32 v10, v10, v11
	v_mul_f32_e32 v11, 0x43800000, v6
	v_mul_f32_e32 v46, 0x43800000, v7
	v_cvt_pk_f16_f32 v11, v11, v46
	ds_read_b128 v[46:49], v74 offset:160
	s_waitcnt lgkmcnt(1)
	v_mfma_f32_32x32x16_f16 a[16:31], v[8:11], v[12:15], a[16:31]
	v_fma_mix_f32 v7, v7, s3, -v11 op_sel:[0,0,1] op_sel_hi:[0,0,1]
	v_fma_mix_f32 v54, v4, s3, -v10 op_sel_hi:[0,0,1]
	v_fma_mix_f32 v55, v5, s3, -v10 op_sel:[0,0,1] op_sel_hi:[0,0,1]
	v_fma_mix_f32 v56, v6, s3, -v11 op_sel_hi:[0,0,1]
	v_cvt_pk_f16_f32 v4, v50, v51
	v_cvt_pk_f16_f32 v5, v52, v53
	v_cvt_pk_f16_f32 v6, v54, v55
	v_cvt_pk_f16_f32 v7, v56, v7
	s_waitcnt vmcnt(5)
	v_mul_f32_e32 v54, 0x43800000, v35
	v_mfma_f32_32x32x16_f16 a[16:31], v[4:7], v[12:15], a[16:31]
	ds_read_b128 v[12:15], v40 offset:128
	ds_read_b128 v[50:53], v40 offset:160
	v_mul_f32_e32 v57, 0x43800000, v135
	s_waitcnt lgkmcnt(1)
	v_mfma_f32_32x32x16_f16 a[16:31], v[8:11], v[12:15], a[16:31]
	s_waitcnt vmcnt(4)
	v_mul_f32_e32 v12, 0x43800000, v36
	v_mul_f32_e32 v13, 0x43800000, v37
	v_mul_f32_e32 v14, 0x43800000, v38
	v_mul_f32_e32 v15, 0x43800000, v39
	v_cvt_pk_f16_f32 v12, v12, v13
	v_cvt_pk_f16_f32 v13, v14, v15
	v_mul_f32_e32 v14, 0x43800000, v32
	v_mul_f32_e32 v15, 0x43800000, v33
	v_cvt_pk_f16_f32 v14, v14, v15
	v_mul_f32_e32 v15, 0x43800000, v34
	v_cvt_pk_f16_f32 v15, v15, v54
	v_fma_mix_f32 v36, v36, s3, -v12 op_sel_hi:[0,0,1]
	v_fma_mix_f32 v35, v35, s3, -v15 op_sel:[0,0,1] op_sel_hi:[0,0,1]
	v_mfma_f32_32x32x16_f16 a[16:31], v[12:15], v[46:49], a[16:31]
	v_fma_mix_f32 v37, v37, s3, -v12 op_sel:[0,0,1] op_sel_hi:[0,0,1]
	v_fma_mix_f32 v38, v38, s3, -v13 op_sel_hi:[0,0,1]
	v_fma_mix_f32 v39, v39, s3, -v13 op_sel:[0,0,1] op_sel_hi:[0,0,1]
	v_fma_mix_f32 v54, v32, s3, -v14 op_sel_hi:[0,0,1]
	v_fma_mix_f32 v55, v33, s3, -v14 op_sel:[0,0,1] op_sel_hi:[0,0,1]
	v_fma_mix_f32 v56, v34, s3, -v15 op_sel_hi:[0,0,1]
	v_cvt_pk_f16_f32 v32, v36, v37
	v_cvt_pk_f16_f32 v33, v38, v39
	v_cvt_pk_f16_f32 v34, v54, v55
	v_cvt_pk_f16_f32 v35, v56, v35
	s_waitcnt vmcnt(2)
	v_mul_f32_e32 v36, 0x43800000, v28
	v_mfma_f32_32x32x16_f16 a[16:31], v[32:35], v[46:49], a[16:31]
	v_mul_f32_e32 v37, 0x43800000, v29
	v_mul_f32_e32 v38, 0x43800000, v30
	v_mul_f32_e32 v39, 0x43800000, v31
	v_cvt_pk_f16_f32 v36, v36, v37
	v_cvt_pk_f16_f32 v37, v38, v39
	v_mul_f32_e32 v38, 0x43800000, v24
	v_mul_f32_e32 v39, 0x43800000, v25
	s_waitcnt lgkmcnt(0)
	v_mfma_f32_32x32x16_f16 a[16:31], v[12:15], v[50:53], a[16:31]
	v_fma_mix_f32 v50, v28, s3, -v36 op_sel_hi:[0,0,1]
	v_fma_mix_f32 v51, v29, s3, -v36 op_sel:[0,0,1] op_sel_hi:[0,0,1]
	v_fma_mix_f32 v52, v30, s3, -v37 op_sel_hi:[0,0,1]
	v_fma_mix_f32 v53, v31, s3, -v37 op_sel:[0,0,1] op_sel_hi:[0,0,1]
	ds_read_b128 v[28:31], v74 offset:192
	v_cvt_pk_f16_f32 v38, v38, v39
	v_mul_f32_e32 v39, 0x43800000, v26
	v_mul_f32_e32 v46, 0x43800000, v27
	v_mfma_f32_32x32x16_f16 a[0:15], v[42:45], v[60:63], a[0:15]
	v_cvt_pk_f16_f32 v39, v39, v46
	ds_read_b128 v[46:49], v74 offset:224
	v_fma_mix_f32 v27, v27, s3, -v39 op_sel:[0,0,1] op_sel_hi:[0,0,1]
	v_fma_mix_f32 v54, v24, s3, -v38 op_sel_hi:[0,0,1]
	v_fma_mix_f32 v55, v25, s3, -v38 op_sel:[0,0,1] op_sel_hi:[0,0,1]
	v_fma_mix_f32 v56, v26, s3, -v39 op_sel_hi:[0,0,1]
	v_cvt_pk_f16_f32 v24, v50, v51
	s_waitcnt lgkmcnt(1)
	v_mfma_f32_32x32x16_f16 a[16:31], v[36:39], v[28:31], a[16:31]
	v_cvt_pk_f16_f32 v25, v52, v53
	v_cvt_pk_f16_f32 v26, v54, v55
	v_cvt_pk_f16_f32 v27, v56, v27
	s_waitcnt vmcnt(1)
	v_mul_f32_e32 v54, 0x43800000, v19
	v_mfma_f32_32x32x16_f16 a[0:15], v[0:3], v[60:63], a[0:15]
	v_mfma_f32_32x32x16_f16 a[16:31], v[24:27], v[28:31], a[16:31]
	ds_read_b128 v[28:31], v40 offset:192
	ds_read_b128 v[50:53], v40 offset:224
	v_mfma_f32_32x32x16_f16 a[0:15], v[42:45], v[64:67], a[0:15]
	v_mov_b32_e32 v44, v158
	v_mov_b32_e32 v42, v159
	s_waitcnt lgkmcnt(1)
	v_mfma_f32_32x32x16_f16 a[16:31], v[36:39], v[28:31], a[16:31]
	s_waitcnt vmcnt(0)
	v_mul_f32_e32 v28, 0x43800000, v20
	v_mul_f32_e32 v29, 0x43800000, v21
	v_mul_f32_e32 v30, 0x43800000, v22
	v_mul_f32_e32 v31, 0x43800000, v23
	v_cvt_pk_f16_f32 v28, v28, v29
	v_cvt_pk_f16_f32 v29, v30, v31
	v_mul_f32_e32 v30, 0x43800000, v16
	v_mul_f32_e32 v31, 0x43800000, v17
	v_fma_mix_f32 v20, v20, s3, -v28 op_sel_hi:[0,0,1]
	v_fma_mix_f32 v21, v21, s3, -v28 op_sel:[0,0,1] op_sel_hi:[0,0,1]
	v_fma_mix_f32 v22, v22, s3, -v29 op_sel_hi:[0,0,1]
	v_fma_mix_f32 v23, v23, s3, -v29 op_sel:[0,0,1] op_sel_hi:[0,0,1]
	v_cvt_pk_f16_f32 v30, v30, v31
	v_mul_f32_e32 v31, 0x43800000, v18
	v_cvt_pk_f16_f32 v31, v31, v54
	v_fma_mix_f32 v54, v16, s3, -v30 op_sel_hi:[0,0,1]
	v_fma_mix_f32 v55, v17, s3, -v30 op_sel:[0,0,1] op_sel_hi:[0,0,1]
	v_cvt_pk_f16_f32 v16, v20, v21
	v_cvt_pk_f16_f32 v17, v22, v23
	ds_read_b128 v[0:3], v74 offset:8832
	ds_read_b128 v[20:23], v74 offset:8864
	s_waitcnt lgkmcnt(1)
	v_mfma_f32_32x32x16_f16 a[0:15], v[8:11], v[0:3], a[0:15]
	v_fma_mix_f32 v19, v19, s3, -v31 op_sel:[0,0,1] op_sel_hi:[0,0,1]
	v_fma_mix_f32 v56, v18, s3, -v31 op_sel_hi:[0,0,1]
	v_cvt_pk_f16_f32 v18, v54, v55
	v_cvt_pk_f16_f32 v19, v56, v19
	v_mul_f32_e32 v54, 0x43800000, v139
	v_mul_f32_e32 v55, 0x43800000, v133
	v_mul_f32_e32 v56, 0x43800000, v134
	v_mfma_f32_32x32x16_f16 a[0:15], v[4:7], v[0:3], a[0:15]
	ds_read_b128 v[0:3], v40 offset:8832
	ds_read_b128 v[4:7], v40 offset:8864
	s_waitcnt lgkmcnt(1)
	v_mfma_f32_32x32x16_f16 a[0:15], v[8:11], v[0:3], a[0:15]
	ds_read_b128 v[0:3], v74 offset:8896
	ds_read_b128 v[8:11], v74 offset:8928
	v_mfma_f32_32x32x16_f16 a[0:15], v[12:15], v[20:23], a[0:15]
	v_mfma_f32_32x32x16_f16 a[0:15], v[32:35], v[20:23], a[0:15]
	v_mov_b32_e32 v32, v155
	v_mov_b32_e32 v34, v154
	s_waitcnt lgkmcnt(2)
	v_mfma_f32_32x32x16_f16 a[0:15], v[12:15], v[4:7], a[0:15]
	ds_read_b128 v[12:15], v40 offset:8896
	ds_read_b128 v[20:23], v40 offset:8928
	s_waitcnt lgkmcnt(0)
	s_barrier
	v_mfma_f32_32x32x16_f16 a[0:15], v[36:39], v[0:3], a[0:15]
	v_mfma_f32_32x32x16_f16 a[0:15], v[24:27], v[0:3], a[0:15]
	v_mov_b32_e32 v26, v148
	v_mov_b32_e32 v24, v149
	v_mfma_f32_32x32x16_f16 a[0:15], v[36:39], v[12:15], a[0:15]
	v_mov_b32_e32 v38, v152
	v_mov_b32_e32 v36, v153
	v_mfma_f32_32x32x16_f16 a[16:31], v[28:31], v[46:49], a[16:31]
	v_mfma_f32_32x32x16_f16 a[0:15], v[28:31], v[8:11], a[0:15]
	v_mfma_f32_32x32x16_f16 a[16:31], v[16:19], v[46:49], a[16:31]
	v_mov_b32_e32 v48, v156
	v_mov_b32_e32 v46, v157
	v_mfma_f32_32x32x16_f16 a[0:15], v[16:19], v[8:11], a[0:15]
	v_mfma_f32_32x32x16_f16 a[16:31], v[28:31], v[50:53], a[16:31]
	v_mul_f32_e32 v50, 0x43800000, v140
	v_mul_f32_e32 v51, 0x43800000, v136
	v_mul_f32_e32 v52, 0x43800000, v137
	v_mul_f32_e32 v53, 0x43800000, v138
	v_mfma_f32_32x32x16_f16 a[0:15], v[28:31], v[20:23], a[0:15]
	s_nop 6
	v_accvgpr_read_b32 v45, a18
	v_accvgpr_read_b32 v47, a17
	v_accvgpr_read_b32 v49, a16
	v_mul_f32_e64 v8, v48, s0
	v_mul_f32_e64 v9, v49, s1
	v_pk_mul_f32 v[10:11], v[46:47], s[0:1]
	v_pk_mul_f32 v[16:17], v[44:45], s[0:1]
	v_add_f32_e32 v0, v8, v9
	v_accvgpr_read_b32 v43, a19
	v_accvgpr_read_b32 v2, a0
	v_accvgpr_read_b32 v4, a1
	v_accvgpr_read_b32 v6, a2
	v_fmac_f32_e32 v8, 0x3b800000, v2
	v_add_f32_e32 v2, v10, v11
	v_fmac_f32_e32 v10, 0x3b800000, v4
	v_add_f32_e32 v4, v16, v17
	v_fmac_f32_e32 v16, 0x3b800000, v6
	v_cvt_pk_f16_f32 v20, v0, v2
	v_pk_mul_f32 v[18:19], v[42:43], s[0:1]
	v_cvt_f32_f16_e32 v6, v20
	v_cvt_f32_f16_sdwa v9, v20 dst_sel:DWORD dst_unused:UNUSED_PAD src0_sel:WORD_1
	v_add_f32_e32 v11, v18, v19
	v_cvt_pk_f16_f32 v21, v4, v11
	v_sub_f32_e32 v0, v0, v6
	v_cvt_f32_f16_e32 v6, v21
	v_sub_f32_e32 v2, v2, v9
	v_cvt_f32_f16_sdwa v9, v21 dst_sel:DWORD dst_unused:UNUSED_PAD src0_sel:WORD_1
	v_cvt_pk_f16_f32 v22, v0, v2
	v_accvgpr_read_b32 v2, a3
	v_sub_f32_e32 v4, v4, v6
	v_cvt_pk_f16_f32 v28, v8, v10
	v_fmac_f32_e32 v18, 0x3b800000, v2
	v_cvt_f32_f16_e32 v0, v28
	v_cvt_f32_f16_sdwa v2, v28 dst_sel:DWORD dst_unused:UNUSED_PAD src0_sel:WORD_1
	v_sub_f32_e32 v6, v11, v9
	v_cvt_pk_f16_f32 v23, v4, v6
	v_cvt_pk_f16_f32 v29, v16, v18
	v_accvgpr_read_b32 v37, a21
	v_cvt_f32_f16_e32 v4, v29
	v_accvgpr_read_b32 v39, a20
	v_sub_f32_e32 v0, v8, v0
	v_cvt_f32_f16_sdwa v6, v29 dst_sel:DWORD dst_unused:UNUSED_PAD src0_sel:WORD_1
	v_sub_f32_e32 v2, v10, v2
	v_accvgpr_read_b32 v33, a23
	v_sub_f32_e32 v4, v16, v4
	v_cvt_pk_f16_f32 v8, v0, v2
	v_lshlrev_b32_e32 v0, 1, v142
	v_pk_mul_f32 v[10:11], v[38:39], s[0:1]
	v_accvgpr_read_b32 v2, a4
	v_pk_mul_f32 v[16:17], v[36:37], s[0:1]
	v_lshl_or_b32 v72, v141, 3, v0
	v_add_f32_e32 v0, v10, v11
	v_fmac_f32_e32 v10, 0x3b800000, v2
	v_add_f32_e32 v2, v16, v17
	v_pk_mul_f32 v[30:31], v[32:33], s[0:1]
	v_cvt_pk_f16_f32 v32, v0, v2
	v_accvgpr_read_b32 v35, a22
	v_cvt_f32_f16_e32 v11, v32
	v_sub_f32_e32 v6, v18, v6
	v_cvt_pk_f16_f32 v9, v4, v6
	v_accvgpr_read_b32 v4, a5
	v_pk_mul_f32 v[18:19], v[34:35], s[0:1]
	v_accvgpr_read_b32 v6, a6
	v_accvgpr_read_b32 v12, a7
	v_fmac_f32_e32 v16, 0x3b800000, v4
	v_add_f32_e32 v4, v18, v19
	v_fmac_f32_e32 v18, 0x3b800000, v6
	v_add_f32_e32 v6, v30, v31
	v_fmac_f32_e32 v30, 0x3b800000, v12
	v_cvt_pk_f16_f32 v33, v4, v6
	v_sub_f32_e32 v0, v0, v11
	v_cvt_f32_f16_sdwa v11, v32 dst_sel:DWORD dst_unused:UNUSED_PAD src0_sel:WORD_1
	v_cvt_f32_f16_e32 v12, v33
	v_cvt_f32_f16_sdwa v14, v33 dst_sel:DWORD dst_unused:UNUSED_PAD src0_sel:WORD_1
	v_cvt_pk_f16_f32 v34, v10, v16
	v_sub_f32_e32 v2, v2, v11
	v_sub_f32_e32 v4, v4, v12
	v_sub_f32_e32 v6, v6, v14
	v_cvt_f32_f16_e32 v11, v34
	v_cvt_pk_f16_f32 v36, v0, v2
	v_cvt_pk_f16_f32 v37, v4, v6
	v_cvt_pk_f16_f32 v35, v18, v30
	v_cvt_f32_f16_sdwa v2, v34 dst_sel:DWORD dst_unused:UNUSED_PAD src0_sel:WORD_1
	v_cvt_f32_f16_e32 v4, v35
	v_cvt_f32_f16_sdwa v6, v35 dst_sel:DWORD dst_unused:UNUSED_PAD src0_sel:WORD_1
	v_mad_u32_u24 v31, v76, s4, v72
	v_add_u32_e32 v38, v41, v72
	v_accvgpr_read_b32 v13, a27
	v_accvgpr_read_b32 v15, a26
	v_accvgpr_read_b32 v25, a25
	v_accvgpr_read_b32 v27, a24
	v_sub_f32_e32 v0, v10, v11
	v_sub_f32_e32 v2, v16, v2
	v_sub_f32_e32 v4, v18, v4
	v_sub_f32_e32 v6, v30, v6
	v_cvt_pk_f16_f32 v10, v0, v2
	v_cvt_pk_f16_f32 v11, v4, v6
	ds_write2_b64 v31, v[20:21], v[32:33] offset1:2
	ds_write2_b64 v38, v[22:23], v[36:37] offset1:2
	v_add_u32_e32 v23, 0x2000, v38
	v_mov_b32_e32 v14, v150
	v_mov_b32_e32 v12, v151
	ds_write2_b64 v23, v[8:9], v[10:11] offset0:64 offset1:66
	v_pk_mul_f32 v[8:9], v[26:27], s[0:1]
	v_accvgpr_read_b32 v2, a8
	v_pk_mul_f32 v[10:11], v[24:25], s[0:1]
	v_accvgpr_read_b32 v4, a9
	v_pk_mul_f32 v[14:15], v[14:15], s[0:1]
	v_accvgpr_read_b32 v6, a10
	v_pk_mul_f32 v[12:13], v[12:13], s[0:1]
	v_add_f32_e32 v0, v8, v9
	v_fmac_f32_e32 v8, 0x3b800000, v2
	v_add_f32_e32 v2, v10, v11
	v_fmac_f32_e32 v10, 0x3b800000, v4
	v_add_f32_e32 v4, v14, v15
	v_fmac_f32_e32 v14, 0x3b800000, v6
	v_add_f32_e32 v6, v12, v13
	v_accvgpr_read_b32 v9, a11
	v_cvt_pk_f16_f32 v17, v4, v6
	v_fmac_f32_e32 v12, 0x3b800000, v9
	v_cvt_f32_f16_sdwa v15, v17 dst_sel:DWORD dst_unused:UNUSED_PAD src0_sel:WORD_1
	v_cvt_pk_f16_f32 v16, v0, v2
	v_cvt_f32_f16_e32 v13, v17
	v_cvt_f32_f16_e32 v9, v16
	v_cvt_f32_f16_sdwa v11, v16 dst_sel:DWORD dst_unused:UNUSED_PAD src0_sel:WORD_1
	v_sub_f32_e32 v6, v6, v15
	v_sub_f32_e32 v4, v4, v13
	v_sub_f32_e32 v0, v0, v9
	v_cvt_pk_f16_f32 v19, v4, v6
	v_cvt_pk_f16_f32 v21, v14, v12
	v_sub_f32_e32 v2, v2, v11
	v_cvt_f32_f16_sdwa v6, v21 dst_sel:DWORD dst_unused:UNUSED_PAD src0_sel:WORD_1
	v_cvt_pk_f16_f32 v18, v0, v2
	v_cvt_pk_f16_f32 v20, v8, v10
	v_cvt_f32_f16_e32 v4, v21
	v_cvt_f32_f16_e32 v0, v20
	v_cvt_f32_f16_sdwa v2, v20 dst_sel:DWORD dst_unused:UNUSED_PAD src0_sel:WORD_1
	v_sub_f32_e32 v6, v12, v6
	v_accvgpr_read_b32 v7, a28
	v_sub_f32_e32 v0, v8, v0
	v_sub_f32_e32 v4, v14, v4
	v_cvt_pk_f16_f32 v9, v4, v6
	v_mov_b32_e32 v6, v144
	v_accvgpr_read_b32 v5, a29
	v_sub_f32_e32 v2, v10, v2
	v_cvt_pk_f16_f32 v8, v0, v2
	v_pk_mul_f32 v[6:7], v[6:7], s[0:1]
	v_accvgpr_read_b32 v0, a12
	v_mov_b32_e32 v4, v145
	v_accvgpr_read_b32 v3, a30
	v_add_f32_e32 v7, v6, v7
	v_fmac_f32_e32 v6, 0x3b800000, v0
	v_pk_mul_f32 v[4:5], v[4:5], s[0:1]
	v_accvgpr_read_b32 v0, a13
	v_mov_b32_e32 v2, v146
	v_add_f32_e32 v5, v4, v5
	v_fmac_f32_e32 v4, 0x3b800000, v0
	v_pk_mul_f32 v[2:3], v[2:3], s[0:1]
	v_accvgpr_read_b32 v0, a14
	v_accvgpr_read_b32 v1, a31
	v_add_f32_e32 v3, v2, v3
	v_fmac_f32_e32 v2, 0x3b800000, v0
	v_mov_b32_e32 v0, v147
	v_pk_mul_f32 v[0:1], v[0:1], s[0:1]
	v_accvgpr_read_b32 v10, a15
	v_add_f32_e32 v1, v0, v1
	v_cvt_pk_f16_f32 v11, v3, v1
	v_fmac_f32_e32 v0, 0x3b800000, v10
	v_cvt_f32_f16_sdwa v15, v11 dst_sel:DWORD dst_unused:UNUSED_PAD src0_sel:WORD_1
	v_cvt_pk_f16_f32 v10, v7, v5
	v_cvt_f32_f16_e32 v14, v11
	v_cvt_f32_f16_e32 v12, v10
	v_cvt_f32_f16_sdwa v13, v10 dst_sel:DWORD dst_unused:UNUSED_PAD src0_sel:WORD_1
	v_sub_f32_e32 v1, v1, v15
	v_sub_f32_e32 v3, v3, v14
	v_sub_f32_e32 v7, v7, v12
	v_sub_f32_e32 v5, v5, v13
	v_cvt_pk_f16_f32 v13, v3, v1
	v_cvt_pk_f16_f32 v14, v6, v4
	v_cvt_pk_f16_f32 v12, v7, v5
	v_cvt_pk_f16_f32 v15, v2, v0
	v_add_u32_e32 v22, 0x2000, v31
	v_cvt_f32_f16_e32 v1, v14
	v_cvt_f32_f16_sdwa v3, v14 dst_sel:DWORD dst_unused:UNUSED_PAD src0_sel:WORD_1
	v_cvt_f32_f16_e32 v5, v15
	v_cvt_f32_f16_sdwa v7, v15 dst_sel:DWORD dst_unused:UNUSED_PAD src0_sel:WORD_1
	v_sub_f32_e32 v1, v6, v1
	v_sub_f32_e32 v3, v4, v3
	v_sub_f32_e32 v2, v2, v5
	v_sub_f32_e32 v4, v0, v7
	v_cvt_pk_f16_f32 v0, v1, v3
	v_cvt_pk_f16_f32 v1, v2, v4
	ds_write2_b64 v22, v[28:29], v[34:35] offset0:64 offset1:66
	ds_write2_b64 v31, v[16:17], v[10:11] offset0:4 offset1:6
	ds_write2_b64 v38, v[18:19], v[12:13] offset0:4 offset1:6
	ds_write2_b64 v22, v[20:21], v[14:15] offset0:68 offset1:70
	ds_write2_b64 v23, v[8:9], v[0:1] offset0:68 offset1:70
	s_waitcnt lgkmcnt(0)
	s_barrier
	ds_read_b128 v[0:3], v74
	ds_read_b128 v[8:11], v74 offset:32
	ds_read_b128 v[12:15], v74 offset:8704
	ds_read_b128 v[16:19], v74 offset:8736
	v_cvt_pk_f16_f32 v4, v50, v51
	v_cvt_pk_f16_f32 v5, v52, v53
	v_cvt_pk_f16_f32 v6, v54, v55
	v_cvt_pk_f16_f32 v7, v56, v57
	v_mul_f32_e32 v28, 0x43800000, v124
	s_waitcnt lgkmcnt(3)
	v_mfma_f32_32x32x16_f16 a[0:15], v[4:7], v[0:3], 0
	v_fma_mix_f32 v20, v140, s3, -v4 op_sel_hi:[0,0,1]
	v_fma_mix_f32 v21, v136, s3, -v4 op_sel:[0,0,1] op_sel_hi:[0,0,1]
	v_fma_mix_f32 v22, v137, s3, -v5 op_sel_hi:[0,0,1]
	v_fma_mix_f32 v23, v138, s3, -v5 op_sel:[0,0,1] op_sel_hi:[0,0,1]
	v_fma_mix_f32 v24, v139, s3, -v6 op_sel_hi:[0,0,1]
	v_fma_mix_f32 v25, v133, s3, -v6 op_sel:[0,0,1] op_sel_hi:[0,0,1]
	v_fma_mix_f32 v26, v134, s3, -v7 op_sel_hi:[0,0,1]
	s_waitcnt lgkmcnt(1)
	v_mfma_f32_32x32x16_f16 a[16:31], v[4:7], v[12:15], 0
	v_fma_mix_f32 v27, v135, s3, -v7 op_sel:[0,0,1] op_sel_hi:[0,0,1]
	v_cvt_pk_f16_f32 v20, v20, v21
	v_cvt_pk_f16_f32 v21, v22, v23
	v_cvt_pk_f16_f32 v22, v24, v25
	v_cvt_pk_f16_f32 v23, v26, v27
	v_mul_f32_e32 v24, 0x43800000, v120
	v_mul_f32_e32 v25, 0x43800000, v121
	v_mfma_f32_32x32x16_f16 a[0:15], v[20:23], v[0:3], a[0:15]
	v_mul_f32_e32 v26, 0x43800000, v122
	v_mul_f32_e32 v27, 0x43800000, v123
	s_mov_b64 s[0:1], 0x2000
	v_mfma_f32_32x32x16_f16 a[16:31], v[20:23], v[12:15], a[16:31]
	ds_read_b128 v[0:3], v40
	ds_read_b128 v[12:15], v40 offset:32
	ds_read_b128 v[20:23], v40 offset:8736
	s_waitcnt lgkmcnt(2)
	v_mfma_f32_32x32x16_f16 a[0:15], v[4:7], v[0:3], a[0:15]
	ds_read_b128 v[0:3], v40 offset:8704
	s_waitcnt lgkmcnt(0)
	v_mfma_f32_32x32x16_f16 a[16:31], v[4:7], v[0:3], a[16:31]
	v_mul_f32_e32 v2, 0x43800000, v117
	v_mul_f32_e32 v3, 0x43800000, v118
	v_mul_f32_e32 v4, 0x43800000, v119
	v_cvt_pk_f16_f32 v0, v24, v25
	v_cvt_pk_f16_f32 v1, v26, v27
	v_cvt_pk_f16_f32 v2, v28, v2
	v_cvt_pk_f16_f32 v3, v3, v4
	v_mul_f32_e32 v28, 0x43800000, v116
	v_mfma_f32_32x32x16_f16 a[0:15], v[0:3], v[8:11], a[0:15]
	v_fma_mix_f32 v4, v120, s3, -v0 op_sel_hi:[0,0,1]
	v_fma_mix_f32 v5, v121, s3, -v0 op_sel:[0,0,1] op_sel_hi:[0,0,1]
	v_fma_mix_f32 v6, v122, s3, -v1 op_sel_hi:[0,0,1]
	v_fma_mix_f32 v7, v123, s3, -v1 op_sel:[0,0,1] op_sel_hi:[0,0,1]
	v_fma_mix_f32 v24, v124, s3, -v2 op_sel_hi:[0,0,1]
	v_fma_mix_f32 v25, v117, s3, -v2 op_sel:[0,0,1] op_sel_hi:[0,0,1]
	v_fma_mix_f32 v26, v118, s3, -v3 op_sel_hi:[0,0,1]
	v_mfma_f32_32x32x16_f16 a[16:31], v[0:3], v[16:19], a[16:31]
	v_fma_mix_f32 v27, v119, s3, -v3 op_sel:[0,0,1] op_sel_hi:[0,0,1]
	v_cvt_pk_f16_f32 v4, v4, v5
	v_cvt_pk_f16_f32 v5, v6, v7
	v_cvt_pk_f16_f32 v6, v24, v25
	v_cvt_pk_f16_f32 v7, v26, v27
	s_nop 0
	v_mfma_f32_32x32x16_f16 a[0:15], v[4:7], v[8:11], a[0:15]
	v_mul_f32_e32 v8, 0x43800000, v131
	v_mul_f32_e32 v9, 0x43800000, v125
	v_mul_f32_e32 v10, 0x43800000, v126
	v_mul_f32_e32 v11, 0x43800000, v127
	v_mfma_f32_32x32x16_f16 a[16:31], v[4:7], v[16:19], a[16:31]
	v_mul_f32_e32 v4, 0x43800000, v132
	v_mul_f32_e32 v5, 0x43800000, v128
	v_mul_f32_e32 v6, 0x43800000, v129
	v_mul_f32_e32 v7, 0x43800000, v130
	v_cvt_pk_f16_f32 v4, v4, v5
	v_cvt_pk_f16_f32 v5, v6, v7
	v_cvt_pk_f16_f32 v6, v8, v9
	v_mfma_f32_32x32x16_f16 a[0:15], v[0:3], v[12:15], a[0:15]
	ds_read_b128 v[12:15], v74 offset:8768
	ds_read_b128 v[16:19], v74 offset:8800
	v_cvt_pk_f16_f32 v7, v10, v11
	ds_read_b128 v[8:11], v74 offset:96
	v_fma_mix_f32 v24, v131, s3, -v6 op_sel_hi:[0,0,1]
	v_fma_mix_f32 v25, v125, s3, -v6 op_sel:[0,0,1] op_sel_hi:[0,0,1]
	v_fma_mix_f32 v26, v126, s3, -v7 op_sel_hi:[0,0,1]
	v_mfma_f32_32x32x16_f16 a[16:31], v[0:3], v[20:23], a[16:31]
	ds_read_b128 v[0:3], v74 offset:64
	v_fma_mix_f32 v20, v132, s3, -v4 op_sel_hi:[0,0,1]
	v_fma_mix_f32 v21, v128, s3, -v4 op_sel:[0,0,1] op_sel_hi:[0,0,1]
	v_fma_mix_f32 v22, v129, s3, -v5 op_sel_hi:[0,0,1]
	v_fma_mix_f32 v23, v130, s3, -v5 op_sel:[0,0,1] op_sel_hi:[0,0,1]
	v_fma_mix_f32 v27, v127, s3, -v7 op_sel:[0,0,1] op_sel_hi:[0,0,1]
	v_cvt_pk_f16_f32 v20, v20, v21
	s_waitcnt lgkmcnt(0)
	v_mfma_f32_32x32x16_f16 a[0:15], v[4:7], v[0:3], a[0:15]
	v_cvt_pk_f16_f32 v21, v22, v23
	v_cvt_pk_f16_f32 v22, v24, v25
	v_cvt_pk_f16_f32 v23, v26, v27
	v_mul_f32_e32 v24, 0x43800000, v112
	v_mul_f32_e32 v25, 0x43800000, v113
	v_mul_f32_e32 v26, 0x43800000, v114
	v_mul_f32_e32 v27, 0x43800000, v115
	v_mfma_f32_32x32x16_f16 a[16:31], v[4:7], v[12:15], a[16:31]
	v_mfma_f32_32x32x16_f16 a[0:15], v[20:23], v[0:3], a[0:15]
	v_mfma_f32_32x32x16_f16 a[16:31], v[20:23], v[12:15], a[16:31]
	ds_read_b128 v[0:3], v40 offset:64
	ds_read_b128 v[12:15], v40 offset:96
	ds_read_b128 v[20:23], v40 offset:8800
	s_waitcnt lgkmcnt(2)
	v_mfma_f32_32x32x16_f16 a[0:15], v[4:7], v[0:3], a[0:15]
	ds_read_b128 v[0:3], v40 offset:8768
	s_waitcnt lgkmcnt(0)
	v_mfma_f32_32x32x16_f16 a[16:31], v[4:7], v[0:3], a[16:31]
	v_mul_f32_e32 v2, 0x43800000, v109
	v_mul_f32_e32 v3, 0x43800000, v110
	v_mul_f32_e32 v4, 0x43800000, v111
	v_cvt_pk_f16_f32 v0, v24, v25
	v_cvt_pk_f16_f32 v1, v26, v27
	v_cvt_pk_f16_f32 v2, v28, v2
	v_cvt_pk_f16_f32 v3, v3, v4
	v_mul_f32_e32 v28, 0x43800000, v95
	v_mfma_f32_32x32x16_f16 a[0:15], v[0:3], v[8:11], a[0:15]
	v_fma_mix_f32 v4, v112, s3, -v0 op_sel_hi:[0,0,1]
	v_fma_mix_f32 v5, v113, s3, -v0 op_sel:[0,0,1] op_sel_hi:[0,0,1]
	v_fma_mix_f32 v6, v114, s3, -v1 op_sel_hi:[0,0,1]
	v_fma_mix_f32 v7, v115, s3, -v1 op_sel:[0,0,1] op_sel_hi:[0,0,1]
	v_fma_mix_f32 v24, v116, s3, -v2 op_sel_hi:[0,0,1]
	v_fma_mix_f32 v25, v109, s3, -v2 op_sel:[0,0,1] op_sel_hi:[0,0,1]
	v_fma_mix_f32 v26, v110, s3, -v3 op_sel_hi:[0,0,1]
	v_mfma_f32_32x32x16_f16 a[16:31], v[0:3], v[16:19], a[16:31]
	v_fma_mix_f32 v27, v111, s3, -v3 op_sel:[0,0,1] op_sel_hi:[0,0,1]
	v_cvt_pk_f16_f32 v4, v4, v5
	v_cvt_pk_f16_f32 v5, v6, v7
	v_cvt_pk_f16_f32 v6, v24, v25
	v_cvt_pk_f16_f32 v7, v26, v27
	s_nop 0
	v_mfma_f32_32x32x16_f16 a[0:15], v[4:7], v[8:11], a[0:15]
	v_mul_f32_e32 v8, 0x43800000, v107
	v_mul_f32_e32 v9, 0x43800000, v101
	v_mul_f32_e32 v10, 0x43800000, v102
	v_mul_f32_e32 v11, 0x43800000, v103
	v_mfma_f32_32x32x16_f16 a[16:31], v[4:7], v[16:19], a[16:31]
	v_mul_f32_e32 v4, 0x43800000, v108
	v_mul_f32_e32 v5, 0x43800000, v104
	v_mul_f32_e32 v6, 0x43800000, v105
	v_mul_f32_e32 v7, 0x43800000, v106
	v_cvt_pk_f16_f32 v4, v4, v5
	v_cvt_pk_f16_f32 v5, v6, v7
	v_cvt_pk_f16_f32 v6, v8, v9
	v_mfma_f32_32x32x16_f16 a[0:15], v[0:3], v[12:15], a[0:15]
	ds_read_b128 v[12:15], v74 offset:8832
	ds_read_b128 v[16:19], v74 offset:8864
	v_cvt_pk_f16_f32 v7, v10, v11
	ds_read_b128 v[8:11], v74 offset:160
	v_fma_mix_f32 v24, v107, s3, -v6 op_sel_hi:[0,0,1]
	v_fma_mix_f32 v25, v101, s3, -v6 op_sel:[0,0,1] op_sel_hi:[0,0,1]
	v_fma_mix_f32 v26, v102, s3, -v7 op_sel_hi:[0,0,1]
	v_mfma_f32_32x32x16_f16 a[16:31], v[0:3], v[20:23], a[16:31]
	ds_read_b128 v[0:3], v74 offset:128
	v_fma_mix_f32 v20, v108, s3, -v4 op_sel_hi:[0,0,1]
	v_fma_mix_f32 v21, v104, s3, -v4 op_sel:[0,0,1] op_sel_hi:[0,0,1]
	v_fma_mix_f32 v22, v105, s3, -v5 op_sel_hi:[0,0,1]
	v_fma_mix_f32 v23, v106, s3, -v5 op_sel:[0,0,1] op_sel_hi:[0,0,1]
	v_fma_mix_f32 v27, v103, s3, -v7 op_sel:[0,0,1] op_sel_hi:[0,0,1]
	v_cvt_pk_f16_f32 v20, v20, v21
	s_waitcnt lgkmcnt(0)
	v_mfma_f32_32x32x16_f16 a[0:15], v[4:7], v[0:3], a[0:15]
	v_cvt_pk_f16_f32 v21, v22, v23
	v_cvt_pk_f16_f32 v22, v24, v25
	v_cvt_pk_f16_f32 v23, v26, v27
	v_mul_f32_e32 v24, 0x43800000, v91
	v_mul_f32_e32 v25, 0x43800000, v92
	v_mul_f32_e32 v26, 0x43800000, v93
	v_mul_f32_e32 v27, 0x43800000, v94
	v_mfma_f32_32x32x16_f16 a[16:31], v[4:7], v[12:15], a[16:31]
	v_mfma_f32_32x32x16_f16 a[0:15], v[20:23], v[0:3], a[0:15]
	v_mfma_f32_32x32x16_f16 a[16:31], v[20:23], v[12:15], a[16:31]
	ds_read_b128 v[0:3], v40 offset:128
	ds_read_b128 v[12:15], v40 offset:160
	ds_read_b128 v[20:23], v40 offset:8864
	s_waitcnt lgkmcnt(2)
	v_mfma_f32_32x32x16_f16 a[0:15], v[4:7], v[0:3], a[0:15]
	ds_read_b128 v[0:3], v40 offset:8832
	s_waitcnt lgkmcnt(0)
	v_mfma_f32_32x32x16_f16 a[16:31], v[4:7], v[0:3], a[16:31]
	v_mul_f32_e32 v2, 0x43800000, v88
	v_mul_f32_e32 v3, 0x43800000, v89
	v_mul_f32_e32 v4, 0x43800000, v90
	v_cvt_pk_f16_f32 v0, v24, v25
	v_cvt_pk_f16_f32 v1, v26, v27
	v_cvt_pk_f16_f32 v2, v28, v2
	v_cvt_pk_f16_f32 v3, v3, v4
	v_mul_f32_e32 v28, 0x43800000, v84
	v_mfma_f32_32x32x16_f16 a[0:15], v[0:3], v[8:11], a[0:15]
	v_fma_mix_f32 v4, v91, s3, -v0 op_sel_hi:[0,0,1]
	v_fma_mix_f32 v5, v92, s3, -v0 op_sel:[0,0,1] op_sel_hi:[0,0,1]
	v_fma_mix_f32 v6, v93, s3, -v1 op_sel_hi:[0,0,1]
	v_fma_mix_f32 v7, v94, s3, -v1 op_sel:[0,0,1] op_sel_hi:[0,0,1]
	v_fma_mix_f32 v24, v95, s3, -v2 op_sel_hi:[0,0,1]
	v_fma_mix_f32 v25, v88, s3, -v2 op_sel:[0,0,1] op_sel_hi:[0,0,1]
	v_fma_mix_f32 v26, v89, s3, -v3 op_sel_hi:[0,0,1]
	v_mfma_f32_32x32x16_f16 a[16:31], v[0:3], v[16:19], a[16:31]
	v_fma_mix_f32 v27, v90, s3, -v3 op_sel:[0,0,1] op_sel_hi:[0,0,1]
	v_cvt_pk_f16_f32 v4, v4, v5
	v_cvt_pk_f16_f32 v5, v6, v7
	v_cvt_pk_f16_f32 v6, v24, v25
	v_cvt_pk_f16_f32 v7, v26, v27
	s_nop 0
	v_mfma_f32_32x32x16_f16 a[0:15], v[4:7], v[8:11], a[0:15]
	v_mul_f32_e32 v8, 0x43800000, v99
	v_mul_f32_e32 v9, 0x43800000, v85
	v_mul_f32_e32 v10, 0x43800000, v86
	v_mul_f32_e32 v11, 0x43800000, v87
	v_mfma_f32_32x32x16_f16 a[16:31], v[4:7], v[16:19], a[16:31]
	v_mul_f32_e32 v4, 0x43800000, v100
	v_mul_f32_e32 v5, 0x43800000, v96
	v_mul_f32_e32 v6, 0x43800000, v97
	v_mul_f32_e32 v7, 0x43800000, v98
	v_cvt_pk_f16_f32 v4, v4, v5
	v_cvt_pk_f16_f32 v5, v6, v7
	v_cvt_pk_f16_f32 v6, v8, v9
	v_mfma_f32_32x32x16_f16 a[0:15], v[0:3], v[12:15], a[0:15]
	ds_read_b128 v[12:15], v74 offset:8896
	ds_read_b128 v[16:19], v74 offset:8928
	v_cvt_pk_f16_f32 v7, v10, v11
	ds_read_b128 v[8:11], v74 offset:224
	v_fma_mix_f32 v24, v99, s3, -v6 op_sel_hi:[0,0,1]
	v_fma_mix_f32 v25, v85, s3, -v6 op_sel:[0,0,1] op_sel_hi:[0,0,1]
	v_fma_mix_f32 v26, v86, s3, -v7 op_sel_hi:[0,0,1]
	v_mfma_f32_32x32x16_f16 a[16:31], v[0:3], v[20:23], a[16:31]
	ds_read_b128 v[0:3], v74 offset:192
	v_fma_mix_f32 v20, v100, s3, -v4 op_sel_hi:[0,0,1]
	v_fma_mix_f32 v21, v96, s3, -v4 op_sel:[0,0,1] op_sel_hi:[0,0,1]
	v_fma_mix_f32 v22, v97, s3, -v5 op_sel_hi:[0,0,1]
	v_fma_mix_f32 v23, v98, s3, -v5 op_sel:[0,0,1] op_sel_hi:[0,0,1]
	v_fma_mix_f32 v27, v87, s3, -v7 op_sel:[0,0,1] op_sel_hi:[0,0,1]
	v_cvt_pk_f16_f32 v20, v20, v21
	s_waitcnt lgkmcnt(0)
	v_mfma_f32_32x32x16_f16 a[0:15], v[4:7], v[0:3], a[0:15]
	v_cvt_pk_f16_f32 v21, v22, v23
	v_cvt_pk_f16_f32 v22, v24, v25
	v_cvt_pk_f16_f32 v23, v26, v27
	v_mul_f32_e32 v24, 0x43800000, v80
	v_mul_f32_e32 v25, 0x43800000, v81
	v_mul_f32_e32 v26, 0x43800000, v82
	v_mul_f32_e32 v27, 0x43800000, v83
	v_mfma_f32_32x32x16_f16 a[16:31], v[4:7], v[12:15], a[16:31]
	v_or_b32_e32 v74, s2, v76
	v_mfma_f32_32x32x16_f16 a[0:15], v[20:23], v[0:3], a[0:15]
	v_mfma_f32_32x32x16_f16 a[16:31], v[20:23], v[12:15], a[16:31]
	ds_read_b128 v[0:3], v40 offset:192
	ds_read_b128 v[12:15], v40 offset:224
	ds_read_b128 v[20:23], v40 offset:8928
	s_waitcnt lgkmcnt(2)
	v_mfma_f32_32x32x16_f16 a[0:15], v[4:7], v[0:3], a[0:15]
	ds_read_b128 v[0:3], v40 offset:8896
	s_waitcnt lgkmcnt(0)
	v_mfma_f32_32x32x16_f16 a[16:31], v[4:7], v[0:3], a[16:31]
	v_mul_f32_e32 v2, 0x43800000, v77
	v_mul_f32_e32 v3, 0x43800000, v78
	v_mul_f32_e32 v4, 0x43800000, v79
	v_cvt_pk_f16_f32 v0, v24, v25
	v_cvt_pk_f16_f32 v1, v26, v27
	v_cvt_pk_f16_f32 v2, v28, v2
	v_cvt_pk_f16_f32 v3, v3, v4
	s_nop 0
	v_mfma_f32_32x32x16_f16 a[0:15], v[0:3], v[8:11], a[0:15]
	v_fma_mix_f32 v4, v80, s3, -v0 op_sel_hi:[0,0,1]
	v_fma_mix_f32 v5, v81, s3, -v0 op_sel:[0,0,1] op_sel_hi:[0,0,1]
	v_fma_mix_f32 v6, v82, s3, -v1 op_sel_hi:[0,0,1]
	v_fma_mix_f32 v7, v83, s3, -v1 op_sel:[0,0,1] op_sel_hi:[0,0,1]
	v_fma_mix_f32 v24, v84, s3, -v2 op_sel_hi:[0,0,1]
	v_fma_mix_f32 v25, v77, s3, -v2 op_sel:[0,0,1] op_sel_hi:[0,0,1]
	v_fma_mix_f32 v26, v78, s3, -v3 op_sel_hi:[0,0,1]
	v_mfma_f32_32x32x16_f16 a[16:31], v[0:3], v[16:19], a[16:31]
	v_fma_mix_f32 v27, v79, s3, -v3 op_sel:[0,0,1] op_sel_hi:[0,0,1]
	v_cvt_pk_f16_f32 v4, v4, v5
	v_cvt_pk_f16_f32 v5, v6, v7
	v_cvt_pk_f16_f32 v6, v24, v25
	v_cvt_pk_f16_f32 v7, v26, v27
	s_nop 0
	v_mfma_f32_32x32x16_f16 a[0:15], v[4:7], v[8:11], a[0:15]
	v_mfma_f32_32x32x16_f16 a[16:31], v[4:7], v[16:19], a[16:31]
	v_mfma_f32_32x32x16_f16 a[0:15], v[0:3], v[12:15], a[0:15]
	v_mfma_f32_32x32x16_f16 a[16:31], v[0:3], v[20:23], a[16:31]
	s_nop 15
	v_and_b32_e32 v10, 31, v187
	v_bfe_u32 v11, v187, 5, 1
	v_lshrrev_b32_e32 v12, 6, v187
	v_and_b32_e32 v13, 63, v187
	v_lshrrev_b32_e32 v14, 2, v13
	v_and_b32_e32 v15, 3, v13
	v_and_b32_e32 v16, 3, v10
	v_lshlrev_b32_e32 v16, 4, v16
	v_lshlrev_b32_e32 v17, 6, v10
	v_lshl_add_u32 v17, v11, 3, v17
	v_lshl_add_u32 v17, v12, 12, v17
	v_add_u32_e32 v17, 0x8800, v17
	v_and_b32_e32 v18, 3, v14
	v_xor_b32_e32 v18, v18, v15
	v_lshlrev_b32_e32 v18, 4, v18
	v_lshl_add_u32 v18, v14, 6, v18
	v_lshl_add_u32 v18, v12, 12, v18
	v_add_u32_e32 v18, 0x8800, v18
	v_add_u32_e32 v22, s2, v14
	v_mov_b32_e32 v23, 0
	v_lshlrev_b64 v[22:23], 8, v[22:23]
	v_lshl_add_u64 v[22:23], v[22:23], 0, s[12:13]
	v_lshlrev_b32_e32 v24, 6, v12
	v_lshl_add_u32 v24, v15, 4, v24
	v_mov_b32_e32 v25, 0
	v_lshl_add_u64 v[22:23], v[22:23], 0, v[24:25]
	s_mov_b64 s[28:29], 0x1000
	v_lshl_add_u64 v[24:25], v[22:23], 0, s[28:29]
	v_lshl_add_u64 v[26:27], v[24:25], 0, s[28:29]
	v_lshl_add_u64 v[28:29], v[26:27], 0, s[28:29]
	v_accvgpr_read_b32 v44, a0
	v_accvgpr_read_b32 v45, a1
	v_accvgpr_read_b32 v46, a2
	v_accvgpr_read_b32 v47, a3
	v_mul_f32_e32 v44, 0x39b8aa3b, v44
	v_mul_f32_e32 v45, 0x39b8aa3b, v45
	v_mul_f32_e32 v46, 0x39b8aa3b, v46
	v_mul_f32_e32 v47, 0x39b8aa3b, v47
	v_cvt_pk_f16_f32 v44, v44, v45
	v_cvt_pk_f16_f32 v45, v46, v47
	v_xor_b32_e32 v48, 0x0, v16
	v_add_u32_e32 v48, v48, v17
	ds_write_b64 v48, v[44:45] offset:0
	v_accvgpr_read_b32 v52, a4
	v_accvgpr_read_b32 v53, a5
	v_accvgpr_read_b32 v54, a6
	v_accvgpr_read_b32 v55, a7
	v_mul_f32_e32 v52, 0x39b8aa3b, v52
	v_mul_f32_e32 v53, 0x39b8aa3b, v53
	v_mul_f32_e32 v54, 0x39b8aa3b, v54
	v_mul_f32_e32 v55, 0x39b8aa3b, v55
	v_cvt_pk_f16_f32 v52, v52, v53
	v_cvt_pk_f16_f32 v53, v54, v55
	v_xor_b32_e32 v56, 0x10, v16
	v_add_u32_e32 v56, v56, v17
	ds_write_b64 v56, v[52:53] offset:0
	v_accvgpr_read_b32 v60, a8
	v_accvgpr_read_b32 v61, a9
	v_accvgpr_read_b32 v62, a10
	v_accvgpr_read_b32 v63, a11
	v_mul_f32_e32 v60, 0x39b8aa3b, v60
	v_mul_f32_e32 v61, 0x39b8aa3b, v61
	v_mul_f32_e32 v62, 0x39b8aa3b, v62
	v_mul_f32_e32 v63, 0x39b8aa3b, v63
	v_cvt_pk_f16_f32 v60, v60, v61
	v_cvt_pk_f16_f32 v61, v62, v63
	v_xor_b32_e32 v64, 0x20, v16
	v_add_u32_e32 v64, v64, v17
	ds_write_b64 v64, v[60:61] offset:0
	v_accvgpr_read_b32 v68, a12
	v_accvgpr_read_b32 v69, a13
	v_accvgpr_read_b32 v70, a14
	v_accvgpr_read_b32 v71, a15
	v_mul_f32_e32 v68, 0x39b8aa3b, v68
	v_mul_f32_e32 v69, 0x39b8aa3b, v69
	v_mul_f32_e32 v70, 0x39b8aa3b, v70
	v_mul_f32_e32 v71, 0x39b8aa3b, v71
	v_cvt_pk_f16_f32 v68, v68, v69
	v_cvt_pk_f16_f32 v69, v70, v71
	v_xor_b32_e32 v72, 0x30, v16
	v_add_u32_e32 v72, v72, v17
	ds_write_b64 v72, v[68:69] offset:0
	v_accvgpr_read_b32 v76, a16
	v_accvgpr_read_b32 v77, a17
	v_accvgpr_read_b32 v78, a18
	v_accvgpr_read_b32 v79, a19
	v_mul_f32_e32 v76, 0x39b8aa3b, v76
	v_mul_f32_e32 v77, 0x39b8aa3b, v77
	v_mul_f32_e32 v78, 0x39b8aa3b, v78
	v_mul_f32_e32 v79, 0x39b8aa3b, v79
	v_cvt_pk_f16_f32 v76, v76, v77
	v_cvt_pk_f16_f32 v77, v78, v79
	v_xor_b32_e32 v80, 0x0, v16
	v_add_u32_e32 v80, v80, v17
	ds_write_b64 v80, v[76:77] offset:2048
	v_accvgpr_read_b32 v84, a20
	v_accvgpr_read_b32 v85, a21
	v_accvgpr_read_b32 v86, a22
	v_accvgpr_read_b32 v87, a23
	v_mul_f32_e32 v84, 0x39b8aa3b, v84
	v_mul_f32_e32 v85, 0x39b8aa3b, v85
	v_mul_f32_e32 v86, 0x39b8aa3b, v86
	v_mul_f32_e32 v87, 0x39b8aa3b, v87
	v_cvt_pk_f16_f32 v84, v84, v85
	v_cvt_pk_f16_f32 v85, v86, v87
	v_xor_b32_e32 v88, 0x10, v16
	v_add_u32_e32 v88, v88, v17
	ds_write_b64 v88, v[84:85] offset:2048
	v_accvgpr_read_b32 v92, a24
	v_accvgpr_read_b32 v93, a25
	v_accvgpr_read_b32 v94, a26
	v_accvgpr_read_b32 v95, a27
	v_mul_f32_e32 v92, 0x39b8aa3b, v92
	v_mul_f32_e32 v93, 0x39b8aa3b, v93
	v_mul_f32_e32 v94, 0x39b8aa3b, v94
	v_mul_f32_e32 v95, 0x39b8aa3b, v95
	v_cvt_pk_f16_f32 v92, v92, v93
	v_cvt_pk_f16_f32 v93, v94, v95
	v_xor_b32_e32 v96, 0x20, v16
	v_add_u32_e32 v96, v96, v17
	ds_write_b64 v96, v[92:93] offset:2048
	v_accvgpr_read_b32 v100, a28
	v_accvgpr_read_b32 v101, a29
	v_accvgpr_read_b32 v102, a30
	v_accvgpr_read_b32 v103, a31
	v_mul_f32_e32 v100, 0x39b8aa3b, v100
	v_mul_f32_e32 v101, 0x39b8aa3b, v101
	v_mul_f32_e32 v102, 0x39b8aa3b, v102
	v_mul_f32_e32 v103, 0x39b8aa3b, v103
	v_cvt_pk_f16_f32 v100, v100, v101
	v_cvt_pk_f16_f32 v101, v102, v103
	v_xor_b32_e32 v104, 0x30, v16
	v_add_u32_e32 v104, v104, v17
	ds_write_b64 v104, v[100:101] offset:2048
	s_waitcnt lgkmcnt(0)
	ds_read_b128 v[30:33], v18 offset:0
	ds_read_b128 v[34:37], v18 offset:1024
	ds_read_b128 v[38:41], v18 offset:2048
	ds_read_b128 v[42:45], v18 offset:3072
	v_lshlrev_b32_e32 v172, 7, v187
	v_min_u32_e32 v172, 0x2680, v172
	v_add_u32_e32 v172, 0x25fc, v172
	global_load_dword v173, v172, s[24:25]
	s_waitcnt lgkmcnt(3)
	global_store_dwordx4 v[22:23], v[30:33], off sc1
	s_waitcnt lgkmcnt(2)
	global_store_dwordx4 v[24:25], v[34:37], off sc1
	s_waitcnt lgkmcnt(1)
	global_store_dwordx4 v[26:27], v[38:41], off sc1
	s_waitcnt lgkmcnt(0)
	global_store_dwordx4 v[28:29], v[42:45], off sc1
	s_endpgm

.LBB1_13:
	s_or_b64 exec, exec, s[2:3]
	v_div_scale_f32 v66, s[0:1], v101, v101, 1.0
	v_rcp_f32_e32 v67, v66
	v_div_scale_f32 v68, vcc, 1.0, v101, 1.0
	v_fma_f32 v70, -v66, v67, 1.0
	v_fmac_f32_e32 v67, v70, v67
	v_mul_f32_e32 v70, v68, v67
	v_fma_f32 v71, -v66, v70, v68
	v_fmac_f32_e32 v70, v71, v67
	v_fma_f32 v66, -v66, v70, v68
	v_div_fmas_f32 v66, v66, v67, v70
	v_div_fixup_f32 v68, v66, v101, 1.0
	v_lshrrev_b32_e32 v70, 4, v161
	v_and_b32_e32 v71, 15, v161
	v_lshrrev_b32_e32 v72, 3, v164
	v_and_b32_e32 v73, 15, v160
	v_xor_b32_e32 v72, v72, v73
	v_lshlrev_b32_e32 v72, 4, v72
	v_add_u32_e32 v73, v162, v160
	v_lshlrev_b32_e32 v73, 8, v73
	v_add_u32_e32 v73, 0x10000, v73
	v_xor_b32_e32 v74, v71, v70
	v_lshlrev_b32_e32 v74, 4, v74
	v_add_u32_e32 v75, v162, v70
	v_lshlrev_b32_e32 v75, 8, v75
	v_add_u32_e32 v75, 0x10000, v75
	v_or_b32_e32 v64, v64, v70
	v_lshlrev_b64 v[76:77], 8, v[64:65]
	v_lshl_add_u64 v[76:77], v[76:77], 0, s[24:25]
	v_lshlrev_b32_e32 v78, 4, v71
	v_mov_b32_e32 v79, 0
	v_lshl_add_u64 v[76:77], v[76:77], 0, v[78:79]
	s_mov_b64 s[2:3], 0x1000
	v_lshl_add_u64 v[78:79], v[76:77], 0, s[2:3]
	v_mul_f32_e32 v48, v68, v48
	v_mul_f32_e32 v49, v68, v49
	v_mul_f32_e32 v50, v68, v50
	v_mul_f32_e32 v51, v68, v51
	v_mul_f32_e32 v52, v68, v52
	v_mul_f32_e32 v53, v68, v53
	v_mul_f32_e32 v54, v68, v54
	v_mul_f32_e32 v55, v68, v55
	v_cvt_pk_f16_f32 v48, v48, v49
	v_cvt_pk_f16_f32 v49, v50, v51
	v_cvt_pk_f16_f32 v50, v52, v53
	v_cvt_pk_f16_f32 v51, v54, v55
	v_xor_b32_e32 v80, 0x0, v72
	v_add_u32_e32 v80, v80, v73
	v_permlane32_swap_b32_e32 v48, v50
	v_permlane32_swap_b32_e32 v49, v51
	ds_write_b128 v80, v[48:51]
	v_mul_f32_e32 v56, v68, v56
	v_mul_f32_e32 v57, v68, v57
	v_mul_f32_e32 v58, v68, v58
	v_mul_f32_e32 v59, v68, v59
	v_mul_f32_e32 v60, v68, v60
	v_mul_f32_e32 v61, v68, v61
	v_mul_f32_e32 v62, v68, v62
	v_mul_f32_e32 v63, v68, v63
	v_cvt_pk_f16_f32 v56, v56, v57
	v_cvt_pk_f16_f32 v57, v58, v59
	v_cvt_pk_f16_f32 v58, v60, v61
	v_cvt_pk_f16_f32 v59, v62, v63
	v_xor_b32_e32 v80, 0x20, v72
	v_add_u32_e32 v80, v80, v73
	v_permlane32_swap_b32_e32 v56, v58
	v_permlane32_swap_b32_e32 v57, v59
	ds_write_b128 v80, v[56:59]
	v_mul_f32_e32 v32, v68, v32
	v_mul_f32_e32 v33, v68, v33
	v_mul_f32_e32 v34, v68, v34
	v_mul_f32_e32 v35, v68, v35
	v_mul_f32_e32 v36, v68, v36
	v_mul_f32_e32 v37, v68, v37
	v_mul_f32_e32 v38, v68, v38
	v_mul_f32_e32 v39, v68, v39
	v_cvt_pk_f16_f32 v32, v32, v33
	v_cvt_pk_f16_f32 v33, v34, v35
	v_cvt_pk_f16_f32 v34, v36, v37
	v_cvt_pk_f16_f32 v35, v38, v39
	v_xor_b32_e32 v80, 0x40, v72
	v_add_u32_e32 v80, v80, v73
	v_permlane32_swap_b32_e32 v32, v34
	v_permlane32_swap_b32_e32 v33, v35
	ds_write_b128 v80, v[32:35]
	v_mul_f32_e32 v40, v68, v40
	v_mul_f32_e32 v41, v68, v41
	v_mul_f32_e32 v42, v68, v42
	v_mul_f32_e32 v43, v68, v43
	v_mul_f32_e32 v44, v68, v44
	v_mul_f32_e32 v45, v68, v45
	v_mul_f32_e32 v46, v68, v46
	v_mul_f32_e32 v47, v68, v47
	v_cvt_pk_f16_f32 v40, v40, v41
	v_cvt_pk_f16_f32 v41, v42, v43
	v_cvt_pk_f16_f32 v42, v44, v45
	v_cvt_pk_f16_f32 v43, v46, v47
	v_xor_b32_e32 v80, 0x60, v72
	v_add_u32_e32 v80, v80, v73
	v_permlane32_swap_b32_e32 v40, v42
	v_permlane32_swap_b32_e32 v41, v43
	ds_write_b128 v80, v[40:43]
	v_mul_f32_e32 v16, v68, v16
	v_mul_f32_e32 v17, v68, v17
	v_mul_f32_e32 v18, v68, v18
	v_mul_f32_e32 v19, v68, v19
	v_mul_f32_e32 v20, v68, v20
	v_mul_f32_e32 v21, v68, v21
	v_mul_f32_e32 v22, v68, v22
	v_mul_f32_e32 v23, v68, v23
	v_cvt_pk_f16_f32 v16, v16, v17
	v_cvt_pk_f16_f32 v17, v18, v19
	v_cvt_pk_f16_f32 v18, v20, v21
	v_cvt_pk_f16_f32 v19, v22, v23
	v_xor_b32_e32 v80, 0x80, v72
	v_add_u32_e32 v80, v80, v73
	v_permlane32_swap_b32_e32 v16, v18
	v_permlane32_swap_b32_e32 v17, v19
	ds_write_b128 v80, v[16:19]
	v_mul_f32_e32 v24, v68, v24
	v_mul_f32_e32 v25, v68, v25
	v_mul_f32_e32 v26, v68, v26
	v_mul_f32_e32 v27, v68, v27
	v_mul_f32_e32 v28, v68, v28
	v_mul_f32_e32 v29, v68, v29
	v_mul_f32_e32 v30, v68, v30
	v_mul_f32_e32 v31, v68, v31
	v_cvt_pk_f16_f32 v24, v24, v25
	v_cvt_pk_f16_f32 v25, v26, v27
	v_cvt_pk_f16_f32 v26, v28, v29
	v_cvt_pk_f16_f32 v27, v30, v31
	v_xor_b32_e32 v80, 0xa0, v72
	v_add_u32_e32 v80, v80, v73
	v_permlane32_swap_b32_e32 v24, v26
	v_permlane32_swap_b32_e32 v25, v27
	ds_write_b128 v80, v[24:27]
	v_mul_f32_e32 v0, v68, v0
	v_mul_f32_e32 v1, v68, v1
	v_mul_f32_e32 v2, v68, v2
	v_mul_f32_e32 v3, v68, v3
	v_mul_f32_e32 v4, v68, v4
	v_mul_f32_e32 v5, v68, v5
	v_mul_f32_e32 v6, v68, v6
	v_mul_f32_e32 v7, v68, v7
	v_cvt_pk_f16_f32 v0, v0, v1
	v_cvt_pk_f16_f32 v1, v2, v3
	v_cvt_pk_f16_f32 v2, v4, v5
	v_cvt_pk_f16_f32 v3, v6, v7
	v_xor_b32_e32 v80, 0xc0, v72
	v_add_u32_e32 v80, v80, v73
	v_permlane32_swap_b32_e32 v0, v2
	v_permlane32_swap_b32_e32 v1, v3
	ds_write_b128 v80, v[0:3]
	v_mul_f32_e32 v8, v68, v8
	v_mul_f32_e32 v9, v68, v9
	v_mul_f32_e32 v10, v68, v10
	v_mul_f32_e32 v11, v68, v11
	v_mul_f32_e32 v12, v68, v12
	v_mul_f32_e32 v13, v68, v13
	v_mul_f32_e32 v14, v68, v14
	v_mul_f32_e32 v15, v68, v15
	v_cvt_pk_f16_f32 v8, v8, v9
	v_cvt_pk_f16_f32 v9, v10, v11
	v_cvt_pk_f16_f32 v10, v12, v13
	v_cvt_pk_f16_f32 v11, v14, v15
	v_xor_b32_e32 v80, 0xe0, v72
	v_add_u32_e32 v80, v80, v73
	v_permlane32_swap_b32_e32 v8, v10
	v_permlane32_swap_b32_e32 v9, v11
	ds_write_b128 v80, v[8:11]
	s_waitcnt lgkmcnt(0)
	v_xor_b32_e32 v81, 0x0, v74
	v_add_u32_e32 v81, v81, v75
	ds_read_b128 v[88:91], v81 offset:0
	v_xor_b32_e32 v81, 0x40, v74
	v_add_u32_e32 v81, v81, v75
	ds_read_b128 v[92:95], v81 offset:1024
	v_xor_b32_e32 v81, 0x80, v74
	v_add_u32_e32 v81, v81, v75
	ds_read_b128 v[96:99], v81 offset:2048
	v_xor_b32_e32 v81, 0xc0, v74
	v_add_u32_e32 v81, v81, v75
	ds_read_b128 v[100:103], v81 offset:3072
	v_xor_b32_e32 v81, 0x0, v74
	v_add_u32_e32 v81, v81, v75
	ds_read_b128 v[104:107], v81 offset:4096
	v_xor_b32_e32 v81, 0x40, v74
	v_add_u32_e32 v81, v81, v75
	ds_read_b128 v[108:111], v81 offset:5120
	v_xor_b32_e32 v81, 0x80, v74
	v_add_u32_e32 v81, v81, v75
	ds_read_b128 v[112:115], v81 offset:6144
	v_xor_b32_e32 v81, 0xc0, v74
	v_add_u32_e32 v81, v81, v75
	ds_read_b128 v[116:119], v81 offset:7168
	v_lshlrev_b32_e32 v240, 7, v161
	v_min_u32_e32 v240, 0x1100, v240
	v_add_u32_e32 v240, 0x26bc, v240
	global_load_dword v241, v240, s[38:39]
	s_waitcnt lgkmcnt(7)
	global_store_dwordx4 v[76:77], v[88:91], off offset:0 sc1
	s_waitcnt lgkmcnt(6)
	global_store_dwordx4 v[76:77], v[92:95], off offset:1024 sc1
	s_waitcnt lgkmcnt(5)
	global_store_dwordx4 v[76:77], v[96:99], off offset:2048 sc1
	s_waitcnt lgkmcnt(4)
	global_store_dwordx4 v[76:77], v[100:103], off offset:3072 sc1
	s_waitcnt lgkmcnt(3)
	global_store_dwordx4 v[78:79], v[104:107], off offset:0 sc1
	s_waitcnt lgkmcnt(2)
	global_store_dwordx4 v[78:79], v[108:111], off offset:1024 sc1
	s_waitcnt lgkmcnt(1)
	global_store_dwordx4 v[78:79], v[112:115], off offset:2048 sc1
	s_waitcnt lgkmcnt(0)
	global_store_dwordx4 v[78:79], v[116:119], off offset:3072 sc1
	s_endpgm
